# baseline (speedup 1.0000x reference)
.LBB3_11:
	s_lshl_b32 s58, s42, 7
	s_add_i32 s59, s41, 0x400
	s_lshr_b32 s59, s59, 6
	s_bfe_u32 s60, s20, 0x1000c
	s_add_i32 s59, s59, s60
	s_lshl_b32 s59, s59, 19
	s_add_u32 s58, s58, s59
	s_add_u32 s58, s56, s58
	s_addc_u32 s59, s57, 0
	s_add_u32 s60, s58, 0x4000
	s_addc_u32 s61, s59, 0
	s_add_u32 s62, s58, 0x100000
	s_addc_u32 s63, s59, 0
	s_add_u32 s64, s62, 0x4000
	s_addc_u32 s65, s63, 0
	s_lshr_b32 s66, s41, 7
	s_bfe_u32 s67, s20, 0x1000c
	s_add_i32 s66, s66, s67
	s_lshl_b32 s66, s66, 14
	s_lshl_b32 s67, s42, 2
	s_add_u32 s66, s66, s67
	s_add_u32 s66, s14, s66
	s_addc_u32 s67, s15, 0
	v_add_u32_e32 v172, s43, v207
	v_pk_fma_f32 v[244:245], v[244:245], -0.5, -0.5 op_sel_hi:[1,0,0]
	v_pk_fma_f32 v[246:247], v[246:247], -0.5, -0.5 op_sel_hi:[1,0,0]
	v_pk_fma_f32 v[248:249], v[248:249], -0.5, -0.5 op_sel_hi:[1,0,0]
	v_pk_fma_f32 v[250:251], v[250:251], -0.5, -0.5 op_sel_hi:[1,0,0]
	v_pk_fma_f32 v[252:253], v[252:253], -0.5, -0.5 op_sel_hi:[1,0,0]
	v_pk_fma_f32 v[254:255], v[254:255], -0.5, -0.5 op_sel_hi:[1,0,0]
	v_pk_fma_f32 v[232:233], v[232:233], -0.5, -0.5 op_sel_hi:[1,0,0]
	v_pk_fma_f32 v[234:235], v[234:235], -0.5, -0.5 op_sel_hi:[1,0,0]
	v_pk_mul_f32 v[134:135], v[244:245], v[246:247]
	v_pk_mul_f32 v[146:147], v[248:249], v[250:251]
	v_pk_mul_f32 v[180:181], v[252:253], v[254:255]
	v_pk_mul_f32 v[236:237], v[232:233], v[234:235]
	v_mul_f32_e32 v188, v134, v135
	v_mul_f32_e32 v190, v146, v147
	v_mul_f32_e32 v189, v180, v181
	v_mul_f32_e32 v191, v236, v237
	v_pk_mul_f32 v[192:193], v[188:189], v[190:191]
	v_mul_f32_e32 v162, v192, v193
	v_rcp_f32_e32 v173, v162
	v_pk_add_f32 v[164:165], v[114:115], v[116:117]
	v_pk_add_f32 v[164:165], v[164:165], v[78:79]
	v_pk_add_f32 v[164:165], v[164:165], v[80:81]
	v_pk_add_f32 v[164:165], v[164:165], v[106:107]
	v_pk_add_f32 v[164:165], v[164:165], v[108:109]
	v_pk_add_f32 v[164:165], v[164:165], v[70:71]
	v_pk_add_f32 v[164:165], v[164:165], v[72:73]
	v_pk_mul_f32 v[230:231], v[172:173], v[192:193] op_sel:[1,1] op_sel_hi:[1,0]
	v_pk_mul_f32 v[192:193], v[230:231], v[190:191]
	v_pk_mul_f32 v[190:191], v[230:231], v[188:189]
	v_pk_mul_f32 v[136:137], v[192:193], v[134:135] op_sel:[0,1] op_sel_hi:[0,0]
	v_pk_mul_f32 v[148:149], v[190:191], v[146:147] op_sel:[0,1] op_sel_hi:[0,0]
	v_pk_mul_f32 v[182:183], v[192:193], v[180:181] op_sel:[1,1] op_sel_hi:[1,0]
	v_pk_mul_f32 v[238:239], v[190:191], v[236:237] op_sel:[1,1] op_sel_hi:[1,0]
	v_pk_fma_f32 v[138:139], v[136:137], v[246:247], 1.0 op_sel_hi:[1,1,0]
	v_pk_fma_f32 v[140:141], v[136:137], v[244:245], 1.0 op_sel_hi:[1,1,0]
	v_pk_fma_f32 v[150:151], v[148:149], v[250:251], 1.0 op_sel_hi:[1,1,0]
	v_pk_fma_f32 v[152:153], v[148:149], v[248:249], 1.0 op_sel_hi:[1,1,0]
	v_pk_fma_f32 v[184:185], v[182:183], v[254:255], 1.0 op_sel_hi:[1,1,0]
	v_pk_fma_f32 v[186:187], v[182:183], v[252:253], 1.0 op_sel_hi:[1,1,0]
	v_pk_fma_f32 v[240:241], v[238:239], v[234:235], 1.0 op_sel_hi:[1,1,0]
	v_pk_fma_f32 v[242:243], v[238:239], v[232:233], 1.0 op_sel_hi:[1,1,0]
	v_cvt_pk_bf16_f32 v154, v138, v139
	v_cvt_pk_bf16_f32 v155, v140, v141
	v_cvt_pk_bf16_f32 v156, v150, v151
	v_cvt_pk_bf16_f32 v157, v152, v153
	v_cvt_pk_bf16_f32 v158, v184, v185
	v_cvt_pk_bf16_f32 v159, v186, v187
	v_cvt_pk_bf16_f32 v160, v240, v241
	v_cvt_pk_bf16_f32 v161, v242, v243
	ds_read_b128 v[114:117], v172
	ds_read_b128 v[78:81], v172 offset:64
	ds_read_b128 v[106:109], v172 offset:128
	ds_read_b128 v[70:73], v172 offset:192
	v_permlane16_swap_b32_e32 v154, v156
	v_permlane16_swap_b32_e32 v155, v157
	s_cmp_gt_u32 s40, 7
	s_cbranch_scc1 .Lg1_pl1
	global_store_dwordx4 v228, v[154:157], s[58:59] nt
	s_branch .Lg1_dn1
.Lg1_pl1:
	global_store_dwordx4 v228, v[154:157], s[58:59] sc0 sc1 nt

.Lg1_noX:
	v_permlane16_swap_b32_e32 v158, v160
	v_permlane16_swap_b32_e32 v159, v161
	s_cmp_gt_u32 s40, 7
	s_cbranch_scc1 .Lg1_pl2
	global_store_dwordx4 v228, v[158:161], s[58:59] offset:128 nt
	s_branch .Lg1_dn2
.Lg1_pl2:
	global_store_dwordx4 v228, v[158:161], s[58:59] offset:128 sc0 sc1 nt
.Lg1_dn2:
	v_exp_f32_e32 v130, v90
	v_exp_f32_e32 v131, v91
	v_exp_f32_e32 v132, v92
	v_exp_f32_e32 v133, v93
	v_exp_f32_e32 v142, v42
	v_exp_f32_e32 v143, v43
	v_exp_f32_e32 v144, v44
	v_exp_f32_e32 v145, v45
	v_exp_f32_e32 v176, v126
	v_exp_f32_e32 v177, v127
	v_exp_f32_e32 v178, v128
	v_exp_f32_e32 v179, v129
	v_exp_f32_e32 v232, v58
	v_exp_f32_e32 v233, v59
	v_exp_f32_e32 v234, v60
	v_exp_f32_e32 v235, v61
	v_pk_fma_f32 v[130:131], v[130:131], -0.5, -0.5 op_sel_hi:[1,0,0]
	v_pk_fma_f32 v[132:133], v[132:133], -0.5, -0.5 op_sel_hi:[1,0,0]
	v_pk_fma_f32 v[142:143], v[142:143], -0.5, -0.5 op_sel_hi:[1,0,0]
	v_pk_fma_f32 v[144:145], v[144:145], -0.5, -0.5 op_sel_hi:[1,0,0]
	v_pk_fma_f32 v[176:177], v[176:177], -0.5, -0.5 op_sel_hi:[1,0,0]
	v_pk_fma_f32 v[178:179], v[178:179], -0.5, -0.5 op_sel_hi:[1,0,0]
	v_pk_fma_f32 v[232:233], v[232:233], -0.5, -0.5 op_sel_hi:[1,0,0]
	v_pk_fma_f32 v[234:235], v[234:235], -0.5, -0.5 op_sel_hi:[1,0,0]
	v_pk_mul_f32 v[134:135], v[130:131], v[132:133]
	v_pk_mul_f32 v[146:147], v[142:143], v[144:145]
	v_pk_mul_f32 v[180:181], v[176:177], v[178:179]
	v_pk_mul_f32 v[236:237], v[232:233], v[234:235]
	v_mul_f32_e32 v188, v134, v135
	v_mul_f32_e32 v190, v146, v147
	v_mul_f32_e32 v189, v180, v181
	v_mul_f32_e32 v191, v236, v237
	v_pk_mul_f32 v[192:193], v[188:189], v[190:191]
	v_mul_f32_e32 v174, v192, v193
	v_rcp_f32_e32 v173, v174
	v_pk_add_f32 v[164:165], v[164:165], v[90:91]
	v_pk_add_f32 v[164:165], v[164:165], v[92:93]
	v_pk_add_f32 v[164:165], v[164:165], v[42:43]
	v_pk_add_f32 v[164:165], v[164:165], v[44:45]
	v_pk_add_f32 v[164:165], v[164:165], v[126:127]
	v_pk_add_f32 v[164:165], v[164:165], v[128:129]
	v_pk_add_f32 v[164:165], v[164:165], v[58:59]
	v_pk_add_f32 v[164:165], v[164:165], v[60:61]
	v_pk_mul_f32 v[230:231], v[172:173], v[192:193] op_sel:[1,1] op_sel_hi:[1,0]
	v_pk_mul_f32 v[192:193], v[230:231], v[190:191]
	v_pk_mul_f32 v[190:191], v[230:231], v[188:189]
	v_pk_mul_f32 v[136:137], v[192:193], v[134:135] op_sel:[0,1] op_sel_hi:[0,0]
	v_pk_mul_f32 v[148:149], v[190:191], v[146:147] op_sel:[0,1] op_sel_hi:[0,0]
	v_pk_mul_f32 v[182:183], v[192:193], v[180:181] op_sel:[1,1] op_sel_hi:[1,0]
	v_pk_mul_f32 v[238:239], v[190:191], v[236:237] op_sel:[1,1] op_sel_hi:[1,0]
	v_pk_fma_f32 v[138:139], v[136:137], v[132:133], 1.0 op_sel_hi:[1,1,0]
	v_pk_fma_f32 v[140:141], v[136:137], v[130:131], 1.0 op_sel_hi:[1,1,0]
	v_pk_fma_f32 v[150:151], v[148:149], v[144:145], 1.0 op_sel_hi:[1,1,0]
	v_pk_fma_f32 v[152:153], v[148:149], v[142:143], 1.0 op_sel_hi:[1,1,0]
	v_pk_fma_f32 v[184:185], v[182:183], v[178:179], 1.0 op_sel_hi:[1,1,0]
	v_pk_fma_f32 v[186:187], v[182:183], v[176:177], 1.0 op_sel_hi:[1,1,0]
	v_pk_fma_f32 v[240:241], v[238:239], v[234:235], 1.0 op_sel_hi:[1,1,0]
	v_pk_fma_f32 v[242:243], v[238:239], v[232:233], 1.0 op_sel_hi:[1,1,0]
	v_cvt_pk_bf16_f32 v154, v138, v139
	v_cvt_pk_bf16_f32 v155, v140, v141
	v_cvt_pk_bf16_f32 v156, v150, v151
	v_cvt_pk_bf16_f32 v157, v152, v153
	v_cvt_pk_bf16_f32 v158, v184, v185
	v_cvt_pk_bf16_f32 v159, v186, v187
	v_cvt_pk_bf16_f32 v160, v240, v241
	v_cvt_pk_bf16_f32 v161, v242, v243
	ds_read_b128 v[90:93], v172 offset:512
	ds_read_b128 v[42:45], v172 offset:576
	ds_read_b128 v[126:129], v172 offset:640
	ds_read_b128 v[58:61], v172 offset:704
	v_permlane16_swap_b32_e32 v154, v156
	v_permlane16_swap_b32_e32 v155, v157
	s_cmp_gt_u32 s40, 7
	s_cbranch_scc1 .Lg1_pl3
	global_store_dwordx4 v228, v[154:157], s[62:63] nt
	s_branch .Lg1_dn3
.Lg1_pl3:
	global_store_dwordx4 v228, v[154:157], s[62:63] sc0 sc1 nt
.Lg1_dn3:
	v_permlane16_swap_b32_e32 v158, v160
	v_permlane16_swap_b32_e32 v159, v161
	s_cmp_gt_u32 s40, 7
	s_cbranch_scc1 .Lg1_pl4
	global_store_dwordx4 v228, v[158:161], s[62:63] offset:128 nt
	s_branch .Lg1_dn4
.Lg1_pl4:
	global_store_dwordx4 v228, v[158:161], s[62:63] offset:128 sc0 sc1 nt
.Lg1_dn4:
	v_log_f32_e32 v166, v162
	v_log_f32_e32 v170, v174
	v_add_f32_e32 v168, v164, v165
	v_mul_f32_e32 v168, 0xbeb17218, v168
	v_add_f32_e32 v166, v166, v170
	v_fmac_f32_e32 v168, 0x3f317218, v166
	v_mov_b32_e32 v169, v168
	s_nop 1
	v_permlane16_swap_b32_e32 v168, v169
	v_add_f32_e32 v168, v168, v169
	v_mov_b32_e32 v169, v168
	s_nop 1
	v_permlane32_swap_b32_e32 v168, v169
	v_add_f32_e32 v168, v168, v169
	s_mov_b64 exec, s[0:1]
	global_store_dword v229, v168, s[66:67]
	s_mov_b64 exec, -1
	v_exp_f32_e32 v130, v110
	v_exp_f32_e32 v131, v111
	v_exp_f32_e32 v132, v112
	v_exp_f32_e32 v133, v113
	v_exp_f32_e32 v142, v74
	v_exp_f32_e32 v143, v75
	v_exp_f32_e32 v144, v76
	v_exp_f32_e32 v145, v77
	v_exp_f32_e32 v176, v102
	v_exp_f32_e32 v177, v103
	v_exp_f32_e32 v178, v104
	v_exp_f32_e32 v179, v105
	v_exp_f32_e32 v232, v66
	v_exp_f32_e32 v233, v67
	v_exp_f32_e32 v234, v68
	v_exp_f32_e32 v235, v69
	v_pk_fma_f32 v[130:131], v[130:131], -0.5, -0.5 op_sel_hi:[1,0,0]
	v_pk_fma_f32 v[132:133], v[132:133], -0.5, -0.5 op_sel_hi:[1,0,0]
	v_pk_fma_f32 v[142:143], v[142:143], -0.5, -0.5 op_sel_hi:[1,0,0]
	v_pk_fma_f32 v[144:145], v[144:145], -0.5, -0.5 op_sel_hi:[1,0,0]
	v_pk_fma_f32 v[176:177], v[176:177], -0.5, -0.5 op_sel_hi:[1,0,0]
	v_pk_fma_f32 v[178:179], v[178:179], -0.5, -0.5 op_sel_hi:[1,0,0]
	v_pk_fma_f32 v[232:233], v[232:233], -0.5, -0.5 op_sel_hi:[1,0,0]
	v_pk_fma_f32 v[234:235], v[234:235], -0.5, -0.5 op_sel_hi:[1,0,0]
	v_pk_mul_f32 v[134:135], v[130:131], v[132:133]
	v_pk_mul_f32 v[146:147], v[142:143], v[144:145]
	v_pk_mul_f32 v[180:181], v[176:177], v[178:179]
	v_pk_mul_f32 v[236:237], v[232:233], v[234:235]
	v_mul_f32_e32 v188, v134, v135
	v_mul_f32_e32 v190, v146, v147
	v_mul_f32_e32 v189, v180, v181
	v_mul_f32_e32 v191, v236, v237
	v_pk_mul_f32 v[192:193], v[188:189], v[190:191]
	v_mul_f32_e32 v162, v192, v193
	v_rcp_f32_e32 v173, v162
	v_pk_add_f32 v[164:165], v[110:111], v[112:113]
	v_pk_add_f32 v[164:165], v[164:165], v[74:75]
	v_pk_add_f32 v[164:165], v[164:165], v[76:77]
	v_pk_add_f32 v[164:165], v[164:165], v[102:103]
	v_pk_add_f32 v[164:165], v[164:165], v[104:105]
	v_pk_add_f32 v[164:165], v[164:165], v[66:67]
	v_pk_add_f32 v[164:165], v[164:165], v[68:69]
	v_pk_mul_f32 v[230:231], v[172:173], v[192:193] op_sel:[1,1] op_sel_hi:[1,0]
	v_pk_mul_f32 v[192:193], v[230:231], v[190:191]
	v_pk_mul_f32 v[190:191], v[230:231], v[188:189]
	v_pk_mul_f32 v[136:137], v[192:193], v[134:135] op_sel:[0,1] op_sel_hi:[0,0]
	v_pk_mul_f32 v[148:149], v[190:191], v[146:147] op_sel:[0,1] op_sel_hi:[0,0]
	v_pk_mul_f32 v[182:183], v[192:193], v[180:181] op_sel:[1,1] op_sel_hi:[1,0]
	v_pk_mul_f32 v[238:239], v[190:191], v[236:237] op_sel:[1,1] op_sel_hi:[1,0]
	v_pk_fma_f32 v[138:139], v[136:137], v[132:133], 1.0 op_sel_hi:[1,1,0]
	v_pk_fma_f32 v[140:141], v[136:137], v[130:131], 1.0 op_sel_hi:[1,1,0]
	v_pk_fma_f32 v[150:151], v[148:149], v[144:145], 1.0 op_sel_hi:[1,1,0]
	v_pk_fma_f32 v[152:153], v[148:149], v[142:143], 1.0 op_sel_hi:[1,1,0]
	v_pk_fma_f32 v[184:185], v[182:183], v[178:179], 1.0 op_sel_hi:[1,1,0]
	v_pk_fma_f32 v[186:187], v[182:183], v[176:177], 1.0 op_sel_hi:[1,1,0]
	v_pk_fma_f32 v[240:241], v[238:239], v[234:235], 1.0 op_sel_hi:[1,1,0]
	v_pk_fma_f32 v[242:243], v[238:239], v[232:233], 1.0 op_sel_hi:[1,1,0]
	v_cvt_pk_bf16_f32 v154, v138, v139
	v_cvt_pk_bf16_f32 v155, v140, v141
	v_cvt_pk_bf16_f32 v156, v150, v151
	v_cvt_pk_bf16_f32 v157, v152, v153
	v_cvt_pk_bf16_f32 v158, v184, v185
	v_cvt_pk_bf16_f32 v159, v186, v187
	v_cvt_pk_bf16_f32 v160, v240, v241
	v_cvt_pk_bf16_f32 v161, v242, v243
	ds_read_b128 v[110:113], v172
	ds_read_b128 v[74:77], v172 offset:64
	ds_read_b128 v[102:105], v172 offset:128
	ds_read_b128 v[66:69], v172 offset:192
	v_permlane16_swap_b32_e32 v154, v156
	v_permlane16_swap_b32_e32 v155, v157
	s_cmp_gt_u32 s40, 7
	s_cbranch_scc1 .Lg1_pl5
	global_store_dwordx4 v228, v[154:157], s[58:59] offset:2048 nt
	s_branch .Lg1_dn5
.Lg1_pl5:
	global_store_dwordx4 v228, v[154:157], s[58:59] offset:2048 sc0 sc1 nt
.Lg1_dn5:
	v_permlane16_swap_b32_e32 v158, v160
	v_permlane16_swap_b32_e32 v159, v161
	s_cmp_gt_u32 s40, 7
	s_cbranch_scc1 .Lg1_pl6
	global_store_dwordx4 v228, v[158:161], s[58:59] offset:2176 nt
	s_branch .Lg1_dn6
.Lg1_pl6:
	global_store_dwordx4 v228, v[158:161], s[58:59] offset:2176 sc0 sc1 nt
.Lg1_dn6:
	v_exp_f32_e32 v130, v86
	v_exp_f32_e32 v131, v87
	v_exp_f32_e32 v132, v88
	v_exp_f32_e32 v133, v89
	v_exp_f32_e32 v142, v38
	v_exp_f32_e32 v143, v39
	v_exp_f32_e32 v144, v40
	v_exp_f32_e32 v145, v41
	v_exp_f32_e32 v176, v122
	v_exp_f32_e32 v177, v123
	v_exp_f32_e32 v178, v124
	v_exp_f32_e32 v179, v125
	v_exp_f32_e32 v232, v50
	v_exp_f32_e32 v233, v51
	v_exp_f32_e32 v234, v52
	v_exp_f32_e32 v235, v53
	v_pk_fma_f32 v[130:131], v[130:131], -0.5, -0.5 op_sel_hi:[1,0,0]
	v_pk_fma_f32 v[132:133], v[132:133], -0.5, -0.5 op_sel_hi:[1,0,0]
	v_pk_fma_f32 v[142:143], v[142:143], -0.5, -0.5 op_sel_hi:[1,0,0]
	v_pk_fma_f32 v[144:145], v[144:145], -0.5, -0.5 op_sel_hi:[1,0,0]
	v_pk_fma_f32 v[176:177], v[176:177], -0.5, -0.5 op_sel_hi:[1,0,0]
	v_pk_fma_f32 v[178:179], v[178:179], -0.5, -0.5 op_sel_hi:[1,0,0]
	v_pk_fma_f32 v[232:233], v[232:233], -0.5, -0.5 op_sel_hi:[1,0,0]
	v_pk_fma_f32 v[234:235], v[234:235], -0.5, -0.5 op_sel_hi:[1,0,0]
	v_pk_mul_f32 v[134:135], v[130:131], v[132:133]
	v_pk_mul_f32 v[146:147], v[142:143], v[144:145]
	v_pk_mul_f32 v[180:181], v[176:177], v[178:179]
	v_pk_mul_f32 v[236:237], v[232:233], v[234:235]
	v_mul_f32_e32 v188, v134, v135
	v_mul_f32_e32 v190, v146, v147
	v_mul_f32_e32 v189, v180, v181
	v_mul_f32_e32 v191, v236, v237
	v_pk_mul_f32 v[192:193], v[188:189], v[190:191]
	v_mul_f32_e32 v174, v192, v193
	v_rcp_f32_e32 v173, v174
	v_pk_add_f32 v[164:165], v[164:165], v[86:87]
	v_pk_add_f32 v[164:165], v[164:165], v[88:89]
	v_pk_add_f32 v[164:165], v[164:165], v[38:39]
	v_pk_add_f32 v[164:165], v[164:165], v[40:41]
	v_pk_add_f32 v[164:165], v[164:165], v[122:123]
	v_pk_add_f32 v[164:165], v[164:165], v[124:125]
	v_pk_add_f32 v[164:165], v[164:165], v[50:51]
	v_pk_add_f32 v[164:165], v[164:165], v[52:53]
	v_pk_mul_f32 v[230:231], v[172:173], v[192:193] op_sel:[1,1] op_sel_hi:[1,0]
	v_pk_mul_f32 v[192:193], v[230:231], v[190:191]
	v_pk_mul_f32 v[190:191], v[230:231], v[188:189]
	v_pk_mul_f32 v[136:137], v[192:193], v[134:135] op_sel:[0,1] op_sel_hi:[0,0]
	v_pk_mul_f32 v[148:149], v[190:191], v[146:147] op_sel:[0,1] op_sel_hi:[0,0]
	v_pk_mul_f32 v[182:183], v[192:193], v[180:181] op_sel:[1,1] op_sel_hi:[1,0]
	v_pk_mul_f32 v[238:239], v[190:191], v[236:237] op_sel:[1,1] op_sel_hi:[1,0]
	v_pk_fma_f32 v[138:139], v[136:137], v[132:133], 1.0 op_sel_hi:[1,1,0]
	v_pk_fma_f32 v[140:141], v[136:137], v[130:131], 1.0 op_sel_hi:[1,1,0]
	v_pk_fma_f32 v[150:151], v[148:149], v[144:145], 1.0 op_sel_hi:[1,1,0]
	v_pk_fma_f32 v[152:153], v[148:149], v[142:143], 1.0 op_sel_hi:[1,1,0]
	v_pk_fma_f32 v[184:185], v[182:183], v[178:179], 1.0 op_sel_hi:[1,1,0]
	v_pk_fma_f32 v[186:187], v[182:183], v[176:177], 1.0 op_sel_hi:[1,1,0]
	v_pk_fma_f32 v[240:241], v[238:239], v[234:235], 1.0 op_sel_hi:[1,1,0]
	v_pk_fma_f32 v[242:243], v[238:239], v[232:233], 1.0 op_sel_hi:[1,1,0]
	v_cvt_pk_bf16_f32 v154, v138, v139
	v_cvt_pk_bf16_f32 v155, v140, v141
	v_cvt_pk_bf16_f32 v156, v150, v151
	v_cvt_pk_bf16_f32 v157, v152, v153
	v_cvt_pk_bf16_f32 v158, v184, v185
	v_cvt_pk_bf16_f32 v159, v186, v187
	v_cvt_pk_bf16_f32 v160, v240, v241
	v_cvt_pk_bf16_f32 v161, v242, v243
	ds_read_b128 v[86:89], v172 offset:512
	ds_read_b128 v[38:41], v172 offset:576
	ds_read_b128 v[122:125], v172 offset:640
	ds_read_b128 v[50:53], v172 offset:704
	v_permlane16_swap_b32_e32 v154, v156
	v_permlane16_swap_b32_e32 v155, v157
	s_cmp_gt_u32 s40, 7
	s_cbranch_scc1 .Lg1_pl7
	global_store_dwordx4 v228, v[154:157], s[62:63] offset:2048 nt
	s_branch .Lg1_dn7
.Lg1_pl7:
	global_store_dwordx4 v228, v[154:157], s[62:63] offset:2048 sc0 sc1 nt
.Lg1_dn7:
	v_permlane16_swap_b32_e32 v158, v160
	v_permlane16_swap_b32_e32 v159, v161
	s_cmp_gt_u32 s40, 7
	s_cbranch_scc1 .Lg1_pl8
	global_store_dwordx4 v228, v[158:161], s[62:63] offset:2176 nt
	s_branch .Lg1_dn8
.Lg1_pl8:
	global_store_dwordx4 v228, v[158:161], s[62:63] offset:2176 sc0 sc1 nt
.Lg1_dn8:
	v_log_f32_e32 v166, v162
	v_log_f32_e32 v170, v174
	v_add_f32_e32 v168, v164, v165
	v_mul_f32_e32 v168, 0xbeb17218, v168
	v_add_f32_e32 v166, v166, v170
	v_fmac_f32_e32 v168, 0x3f317218, v166
	v_mov_b32_e32 v169, v168
	s_nop 1
	v_permlane16_swap_b32_e32 v168, v169
	v_add_f32_e32 v168, v168, v169
	v_mov_b32_e32 v169, v168
	s_nop 1
	v_permlane32_swap_b32_e32 v168, v169
	v_add_f32_e32 v168, v168, v169
	s_mov_b64 exec, s[0:1]
	global_store_dword v229, v168, s[66:67] offset:64
	s_mov_b64 exec, -1
	v_exp_f32_e32 v130, v98
	v_exp_f32_e32 v131, v99
	v_exp_f32_e32 v132, v100
	v_exp_f32_e32 v133, v101
	v_exp_f32_e32 v142, v62
	v_exp_f32_e32 v143, v63
	v_exp_f32_e32 v144, v64
	v_exp_f32_e32 v145, v65
	v_exp_f32_e32 v176, v94
	v_exp_f32_e32 v177, v95
	v_exp_f32_e32 v178, v96
	v_exp_f32_e32 v179, v97
	v_exp_f32_e32 v232, v54
	v_exp_f32_e32 v233, v55
	v_exp_f32_e32 v234, v56
	v_exp_f32_e32 v235, v57
	v_pk_fma_f32 v[130:131], v[130:131], -0.5, -0.5 op_sel_hi:[1,0,0]
	v_pk_fma_f32 v[132:133], v[132:133], -0.5, -0.5 op_sel_hi:[1,0,0]
	v_pk_fma_f32 v[142:143], v[142:143], -0.5, -0.5 op_sel_hi:[1,0,0]
	v_pk_fma_f32 v[144:145], v[144:145], -0.5, -0.5 op_sel_hi:[1,0,0]
	v_pk_fma_f32 v[176:177], v[176:177], -0.5, -0.5 op_sel_hi:[1,0,0]
	v_pk_fma_f32 v[178:179], v[178:179], -0.5, -0.5 op_sel_hi:[1,0,0]
	v_pk_fma_f32 v[232:233], v[232:233], -0.5, -0.5 op_sel_hi:[1,0,0]
	v_pk_fma_f32 v[234:235], v[234:235], -0.5, -0.5 op_sel_hi:[1,0,0]
	v_pk_mul_f32 v[134:135], v[130:131], v[132:133]
	v_pk_mul_f32 v[146:147], v[142:143], v[144:145]
	v_pk_mul_f32 v[180:181], v[176:177], v[178:179]
	v_pk_mul_f32 v[236:237], v[232:233], v[234:235]
	v_mul_f32_e32 v188, v134, v135
	v_mul_f32_e32 v190, v146, v147
	v_mul_f32_e32 v189, v180, v181
	v_mul_f32_e32 v191, v236, v237
	v_pk_mul_f32 v[192:193], v[188:189], v[190:191]
	v_mul_f32_e32 v162, v192, v193
	v_rcp_f32_e32 v173, v162
	v_pk_add_f32 v[164:165], v[98:99], v[100:101]
	v_pk_add_f32 v[164:165], v[164:165], v[62:63]
	v_pk_add_f32 v[164:165], v[164:165], v[64:65]
	v_pk_add_f32 v[164:165], v[164:165], v[94:95]
	v_pk_add_f32 v[164:165], v[164:165], v[96:97]
	v_pk_add_f32 v[164:165], v[164:165], v[54:55]
	v_pk_add_f32 v[164:165], v[164:165], v[56:57]
	v_pk_mul_f32 v[230:231], v[172:173], v[192:193] op_sel:[1,1] op_sel_hi:[1,0]
	v_pk_mul_f32 v[192:193], v[230:231], v[190:191]
	v_pk_mul_f32 v[190:191], v[230:231], v[188:189]
	v_pk_mul_f32 v[136:137], v[192:193], v[134:135] op_sel:[0,1] op_sel_hi:[0,0]
	v_pk_mul_f32 v[148:149], v[190:191], v[146:147] op_sel:[0,1] op_sel_hi:[0,0]
	v_pk_mul_f32 v[182:183], v[192:193], v[180:181] op_sel:[1,1] op_sel_hi:[1,0]
	v_pk_mul_f32 v[238:239], v[190:191], v[236:237] op_sel:[1,1] op_sel_hi:[1,0]
	v_pk_fma_f32 v[138:139], v[136:137], v[132:133], 1.0 op_sel_hi:[1,1,0]
	v_pk_fma_f32 v[140:141], v[136:137], v[130:131], 1.0 op_sel_hi:[1,1,0]
	v_pk_fma_f32 v[150:151], v[148:149], v[144:145], 1.0 op_sel_hi:[1,1,0]
	v_pk_fma_f32 v[152:153], v[148:149], v[142:143], 1.0 op_sel_hi:[1,1,0]
	v_pk_fma_f32 v[184:185], v[182:183], v[178:179], 1.0 op_sel_hi:[1,1,0]
	v_pk_fma_f32 v[186:187], v[182:183], v[176:177], 1.0 op_sel_hi:[1,1,0]
	v_pk_fma_f32 v[240:241], v[238:239], v[234:235], 1.0 op_sel_hi:[1,1,0]
	v_pk_fma_f32 v[242:243], v[238:239], v[232:233], 1.0 op_sel_hi:[1,1,0]
	v_cvt_pk_bf16_f32 v154, v138, v139
	v_cvt_pk_bf16_f32 v155, v140, v141
	v_cvt_pk_bf16_f32 v156, v150, v151
	v_cvt_pk_bf16_f32 v157, v152, v153
	v_cvt_pk_bf16_f32 v158, v184, v185
	v_cvt_pk_bf16_f32 v159, v186, v187
	v_cvt_pk_bf16_f32 v160, v240, v241
	v_cvt_pk_bf16_f32 v161, v242, v243
	ds_read_b128 v[98:101], v172
	ds_read_b128 v[62:65], v172 offset:64
	ds_read_b128 v[94:97], v172 offset:128
	ds_read_b128 v[54:57], v172 offset:192
	v_permlane16_swap_b32_e32 v154, v156
	v_permlane16_swap_b32_e32 v155, v157
	s_cmp_gt_u32 s40, 7
	s_cbranch_scc1 .Lg1_pl9
	global_store_dwordx4 v228, v[154:157], s[60:61] nt
	s_branch .Lg1_dn9
.Lg1_pl9:
	global_store_dwordx4 v228, v[154:157], s[60:61] sc0 sc1 nt
.Lg1_dn9:
	v_permlane16_swap_b32_e32 v158, v160
	v_permlane16_swap_b32_e32 v159, v161
	s_cmp_gt_u32 s40, 7
	s_cbranch_scc1 .Lg1_pl10
	global_store_dwordx4 v228, v[158:161], s[60:61] offset:128 nt
	s_branch .Lg1_dn10
.Lg1_pl10:
	global_store_dwordx4 v228, v[158:161], s[60:61] offset:128 sc0 sc1 nt
.Lg1_dn10:
	v_exp_f32_e32 v130, v82
	v_exp_f32_e32 v131, v83
	v_exp_f32_e32 v132, v84
	v_exp_f32_e32 v133, v85
	v_exp_f32_e32 v142, v34
	v_exp_f32_e32 v143, v35
	v_exp_f32_e32 v144, v36
	v_exp_f32_e32 v145, v37
	v_exp_f32_e32 v176, v118
	v_exp_f32_e32 v177, v119
	v_exp_f32_e32 v178, v120
	v_exp_f32_e32 v179, v121
	v_exp_f32_e32 v232, v46
	v_exp_f32_e32 v233, v47
	v_exp_f32_e32 v234, v48
	v_exp_f32_e32 v235, v49
	v_pk_fma_f32 v[130:131], v[130:131], -0.5, -0.5 op_sel_hi:[1,0,0]
	v_pk_fma_f32 v[132:133], v[132:133], -0.5, -0.5 op_sel_hi:[1,0,0]
	v_pk_fma_f32 v[142:143], v[142:143], -0.5, -0.5 op_sel_hi:[1,0,0]
	v_pk_fma_f32 v[144:145], v[144:145], -0.5, -0.5 op_sel_hi:[1,0,0]
	v_pk_fma_f32 v[176:177], v[176:177], -0.5, -0.5 op_sel_hi:[1,0,0]
	v_pk_fma_f32 v[178:179], v[178:179], -0.5, -0.5 op_sel_hi:[1,0,0]
	v_pk_fma_f32 v[232:233], v[232:233], -0.5, -0.5 op_sel_hi:[1,0,0]
	v_pk_fma_f32 v[234:235], v[234:235], -0.5, -0.5 op_sel_hi:[1,0,0]
	v_pk_mul_f32 v[134:135], v[130:131], v[132:133]
	v_pk_mul_f32 v[146:147], v[142:143], v[144:145]
	v_pk_mul_f32 v[180:181], v[176:177], v[178:179]
	v_pk_mul_f32 v[236:237], v[232:233], v[234:235]
	v_mul_f32_e32 v188, v134, v135
	v_mul_f32_e32 v190, v146, v147
	v_mul_f32_e32 v189, v180, v181
	v_mul_f32_e32 v191, v236, v237
	v_pk_mul_f32 v[192:193], v[188:189], v[190:191]
	v_mul_f32_e32 v174, v192, v193
	v_rcp_f32_e32 v173, v174
	v_pk_add_f32 v[164:165], v[164:165], v[82:83]
	v_pk_add_f32 v[164:165], v[164:165], v[84:85]
	v_pk_add_f32 v[164:165], v[164:165], v[34:35]
	v_pk_add_f32 v[164:165], v[164:165], v[36:37]
	v_pk_add_f32 v[164:165], v[164:165], v[118:119]
	v_pk_add_f32 v[164:165], v[164:165], v[120:121]
	v_pk_add_f32 v[164:165], v[164:165], v[46:47]
	v_pk_add_f32 v[164:165], v[164:165], v[48:49]
	v_pk_mul_f32 v[230:231], v[172:173], v[192:193] op_sel:[1,1] op_sel_hi:[1,0]
	v_pk_mul_f32 v[192:193], v[230:231], v[190:191]
	v_pk_mul_f32 v[190:191], v[230:231], v[188:189]
	v_pk_mul_f32 v[136:137], v[192:193], v[134:135] op_sel:[0,1] op_sel_hi:[0,0]
	v_pk_mul_f32 v[148:149], v[190:191], v[146:147] op_sel:[0,1] op_sel_hi:[0,0]
	v_pk_mul_f32 v[182:183], v[192:193], v[180:181] op_sel:[1,1] op_sel_hi:[1,0]
	v_pk_mul_f32 v[238:239], v[190:191], v[236:237] op_sel:[1,1] op_sel_hi:[1,0]
	v_pk_fma_f32 v[138:139], v[136:137], v[132:133], 1.0 op_sel_hi:[1,1,0]
	v_pk_fma_f32 v[140:141], v[136:137], v[130:131], 1.0 op_sel_hi:[1,1,0]
	v_pk_fma_f32 v[150:151], v[148:149], v[144:145], 1.0 op_sel_hi:[1,1,0]
	v_pk_fma_f32 v[152:153], v[148:149], v[142:143], 1.0 op_sel_hi:[1,1,0]
	v_pk_fma_f32 v[184:185], v[182:183], v[178:179], 1.0 op_sel_hi:[1,1,0]
	v_pk_fma_f32 v[186:187], v[182:183], v[176:177], 1.0 op_sel_hi:[1,1,0]
	v_pk_fma_f32 v[240:241], v[238:239], v[234:235], 1.0 op_sel_hi:[1,1,0]
	v_pk_fma_f32 v[242:243], v[238:239], v[232:233], 1.0 op_sel_hi:[1,1,0]
	v_cvt_pk_bf16_f32 v154, v138, v139
	v_cvt_pk_bf16_f32 v155, v140, v141
	v_cvt_pk_bf16_f32 v156, v150, v151
	v_cvt_pk_bf16_f32 v157, v152, v153
	v_cvt_pk_bf16_f32 v158, v184, v185
	v_cvt_pk_bf16_f32 v159, v186, v187
	v_cvt_pk_bf16_f32 v160, v240, v241
	v_cvt_pk_bf16_f32 v161, v242, v243
	ds_read_b128 v[82:85], v172 offset:512
	ds_read_b128 v[34:37], v172 offset:576
	ds_read_b128 v[118:121], v172 offset:640
	ds_read_b128 v[46:49], v172 offset:704
	v_permlane16_swap_b32_e32 v154, v156
	v_permlane16_swap_b32_e32 v155, v157
	s_cmp_gt_u32 s40, 7
	s_cbranch_scc1 .Lg1_pl11
	global_store_dwordx4 v228, v[154:157], s[64:65] nt
	s_branch .Lg1_dn11
.Lg1_pl11:
	global_store_dwordx4 v228, v[154:157], s[64:65] sc0 sc1 nt
.Lg1_dn11:
	v_permlane16_swap_b32_e32 v158, v160
	v_permlane16_swap_b32_e32 v159, v161
	s_cmp_gt_u32 s40, 7
	s_cbranch_scc1 .Lg1_pl12
	global_store_dwordx4 v228, v[158:161], s[64:65] offset:128 nt
	s_branch .Lg1_dn12
.Lg1_pl12:
	global_store_dwordx4 v228, v[158:161], s[64:65] offset:128 sc0 sc1 nt
.Lg1_dn12:
	v_log_f32_e32 v166, v162
	v_log_f32_e32 v170, v174
	v_add_f32_e32 v168, v164, v165
	v_mul_f32_e32 v168, 0xbeb17218, v168
	v_add_f32_e32 v166, v166, v170
	v_fmac_f32_e32 v168, 0x3f317218, v166
	v_mov_b32_e32 v169, v168
	s_nop 1
	v_permlane16_swap_b32_e32 v168, v169
	v_add_f32_e32 v168, v168, v169
	v_mov_b32_e32 v169, v168
	s_nop 1
	v_permlane32_swap_b32_e32 v168, v169
	v_add_f32_e32 v168, v168, v169
	s_mov_b64 exec, s[0:1]
	global_store_dword v229, v168, s[66:67] offset:512
	s_mov_b64 exec, -1
	v_exp_f32_e32 v130, v18
	v_exp_f32_e32 v131, v19
	v_exp_f32_e32 v132, v20
	v_exp_f32_e32 v133, v21
	v_exp_f32_e32 v142, v2
	v_exp_f32_e32 v143, v3
	v_exp_f32_e32 v144, v4
	v_exp_f32_e32 v145, v5
	v_exp_f32_e32 v176, v26
	v_exp_f32_e32 v177, v27
	v_exp_f32_e32 v178, v28
	v_exp_f32_e32 v179, v29
	v_exp_f32_e32 v232, v10
	v_exp_f32_e32 v233, v11
	v_exp_f32_e32 v234, v12
	v_exp_f32_e32 v235, v13
	v_pk_fma_f32 v[130:131], v[130:131], -0.5, -0.5 op_sel_hi:[1,0,0]
	v_pk_fma_f32 v[132:133], v[132:133], -0.5, -0.5 op_sel_hi:[1,0,0]
	v_pk_fma_f32 v[142:143], v[142:143], -0.5, -0.5 op_sel_hi:[1,0,0]
	v_pk_fma_f32 v[144:145], v[144:145], -0.5, -0.5 op_sel_hi:[1,0,0]
	v_pk_fma_f32 v[176:177], v[176:177], -0.5, -0.5 op_sel_hi:[1,0,0]
	v_pk_fma_f32 v[178:179], v[178:179], -0.5, -0.5 op_sel_hi:[1,0,0]
	v_pk_fma_f32 v[232:233], v[232:233], -0.5, -0.5 op_sel_hi:[1,0,0]
	v_pk_fma_f32 v[234:235], v[234:235], -0.5, -0.5 op_sel_hi:[1,0,0]
	v_pk_mul_f32 v[134:135], v[130:131], v[132:133]
	v_pk_mul_f32 v[146:147], v[142:143], v[144:145]
	v_pk_mul_f32 v[180:181], v[176:177], v[178:179]
	v_pk_mul_f32 v[236:237], v[232:233], v[234:235]
	v_mul_f32_e32 v188, v134, v135
	v_mul_f32_e32 v190, v146, v147
	v_mul_f32_e32 v189, v180, v181
	v_mul_f32_e32 v191, v236, v237
	v_pk_mul_f32 v[192:193], v[188:189], v[190:191]
	v_mul_f32_e32 v162, v192, v193
	v_rcp_f32_e32 v173, v162
	v_pk_add_f32 v[164:165], v[18:19], v[20:21]
	v_pk_add_f32 v[164:165], v[164:165], v[2:3]
	v_pk_add_f32 v[164:165], v[164:165], v[4:5]
	v_pk_add_f32 v[164:165], v[164:165], v[26:27]
	v_pk_add_f32 v[164:165], v[164:165], v[28:29]
	v_pk_add_f32 v[164:165], v[164:165], v[10:11]
	v_pk_add_f32 v[164:165], v[164:165], v[12:13]
	v_pk_mul_f32 v[230:231], v[172:173], v[192:193] op_sel:[1,1] op_sel_hi:[1,0]
	v_pk_mul_f32 v[192:193], v[230:231], v[190:191]
	v_pk_mul_f32 v[190:191], v[230:231], v[188:189]
	v_pk_mul_f32 v[136:137], v[192:193], v[134:135] op_sel:[0,1] op_sel_hi:[0,0]
	v_pk_mul_f32 v[148:149], v[190:191], v[146:147] op_sel:[0,1] op_sel_hi:[0,0]
	v_pk_mul_f32 v[182:183], v[192:193], v[180:181] op_sel:[1,1] op_sel_hi:[1,0]
	v_pk_mul_f32 v[238:239], v[190:191], v[236:237] op_sel:[1,1] op_sel_hi:[1,0]
	v_pk_fma_f32 v[138:139], v[136:137], v[132:133], 1.0 op_sel_hi:[1,1,0]
	v_pk_fma_f32 v[140:141], v[136:137], v[130:131], 1.0 op_sel_hi:[1,1,0]
	v_pk_fma_f32 v[150:151], v[148:149], v[144:145], 1.0 op_sel_hi:[1,1,0]
	v_pk_fma_f32 v[152:153], v[148:149], v[142:143], 1.0 op_sel_hi:[1,1,0]
	v_pk_fma_f32 v[184:185], v[182:183], v[178:179], 1.0 op_sel_hi:[1,1,0]
	v_pk_fma_f32 v[186:187], v[182:183], v[176:177], 1.0 op_sel_hi:[1,1,0]
	v_pk_fma_f32 v[240:241], v[238:239], v[234:235], 1.0 op_sel_hi:[1,1,0]
	v_pk_fma_f32 v[242:243], v[238:239], v[232:233], 1.0 op_sel_hi:[1,1,0]
	v_cvt_pk_bf16_f32 v154, v138, v139
	v_cvt_pk_bf16_f32 v155, v140, v141
	v_cvt_pk_bf16_f32 v156, v150, v151
	v_cvt_pk_bf16_f32 v157, v152, v153
	v_cvt_pk_bf16_f32 v158, v184, v185
	v_cvt_pk_bf16_f32 v159, v186, v187
	v_cvt_pk_bf16_f32 v160, v240, v241
	v_cvt_pk_bf16_f32 v161, v242, v243
	ds_read_b128 v[18:21], v172
	ds_read_b128 v[2:5], v172 offset:64
	ds_read_b128 v[26:29], v172 offset:128
	ds_read_b128 v[10:13], v172 offset:192
	v_permlane16_swap_b32_e32 v154, v156
	v_permlane16_swap_b32_e32 v155, v157
	s_cmp_gt_u32 s40, 7
	s_cbranch_scc1 .Lg1_pl13
	global_store_dwordx4 v228, v[154:157], s[60:61] offset:2048 nt
	s_branch .Lg1_dn13
.Lg1_pl13:
	global_store_dwordx4 v228, v[154:157], s[60:61] offset:2048 sc0 sc1 nt
.Lg1_dn13:
	v_permlane16_swap_b32_e32 v158, v160
	v_permlane16_swap_b32_e32 v159, v161
	s_cmp_gt_u32 s40, 7
	s_cbranch_scc1 .Lg1_pl14
	global_store_dwordx4 v228, v[158:161], s[60:61] offset:2176 nt
	s_branch .Lg1_dn14
.Lg1_pl14:
	global_store_dwordx4 v228, v[158:161], s[60:61] offset:2176 sc0 sc1 nt
.Lg1_dn14:
	v_exp_f32_e32 v130, v22
	v_exp_f32_e32 v131, v23
	v_exp_f32_e32 v132, v24
	v_exp_f32_e32 v133, v25
	v_exp_f32_e32 v142, v6
	v_exp_f32_e32 v143, v7
	v_exp_f32_e32 v144, v8
	v_exp_f32_e32 v145, v9
	v_exp_f32_e32 v176, v30
	v_exp_f32_e32 v177, v31
	v_exp_f32_e32 v178, v32
	v_exp_f32_e32 v179, v33
	v_exp_f32_e32 v232, v14
	v_exp_f32_e32 v233, v15
	v_exp_f32_e32 v234, v16
	v_exp_f32_e32 v235, v17
	v_pk_fma_f32 v[130:131], v[130:131], -0.5, -0.5 op_sel_hi:[1,0,0]
	v_pk_fma_f32 v[132:133], v[132:133], -0.5, -0.5 op_sel_hi:[1,0,0]
	v_pk_fma_f32 v[142:143], v[142:143], -0.5, -0.5 op_sel_hi:[1,0,0]
	v_pk_fma_f32 v[144:145], v[144:145], -0.5, -0.5 op_sel_hi:[1,0,0]
	v_pk_fma_f32 v[176:177], v[176:177], -0.5, -0.5 op_sel_hi:[1,0,0]
	v_pk_fma_f32 v[178:179], v[178:179], -0.5, -0.5 op_sel_hi:[1,0,0]
	v_pk_fma_f32 v[232:233], v[232:233], -0.5, -0.5 op_sel_hi:[1,0,0]
	v_pk_fma_f32 v[234:235], v[234:235], -0.5, -0.5 op_sel_hi:[1,0,0]
	v_pk_mul_f32 v[134:135], v[130:131], v[132:133]
	v_pk_mul_f32 v[146:147], v[142:143], v[144:145]
	v_pk_mul_f32 v[180:181], v[176:177], v[178:179]
	v_pk_mul_f32 v[236:237], v[232:233], v[234:235]
	v_mul_f32_e32 v188, v134, v135
	v_mul_f32_e32 v190, v146, v147
	v_mul_f32_e32 v189, v180, v181
	v_mul_f32_e32 v191, v236, v237
	v_pk_mul_f32 v[192:193], v[188:189], v[190:191]
	v_mul_f32_e32 v174, v192, v193
	v_rcp_f32_e32 v173, v174
	v_pk_add_f32 v[164:165], v[164:165], v[22:23]
	v_pk_add_f32 v[164:165], v[164:165], v[24:25]
	v_pk_add_f32 v[164:165], v[164:165], v[6:7]
	v_pk_add_f32 v[164:165], v[164:165], v[8:9]
	v_pk_add_f32 v[164:165], v[164:165], v[30:31]
	v_pk_add_f32 v[164:165], v[164:165], v[32:33]
	v_pk_add_f32 v[164:165], v[164:165], v[14:15]
	v_pk_add_f32 v[164:165], v[164:165], v[16:17]
	v_pk_mul_f32 v[230:231], v[172:173], v[192:193] op_sel:[1,1] op_sel_hi:[1,0]
	v_pk_mul_f32 v[192:193], v[230:231], v[190:191]
	v_pk_mul_f32 v[190:191], v[230:231], v[188:189]
	v_pk_mul_f32 v[136:137], v[192:193], v[134:135] op_sel:[0,1] op_sel_hi:[0,0]
	v_pk_mul_f32 v[148:149], v[190:191], v[146:147] op_sel:[0,1] op_sel_hi:[0,0]
	v_pk_mul_f32 v[182:183], v[192:193], v[180:181] op_sel:[1,1] op_sel_hi:[1,0]
	v_pk_mul_f32 v[238:239], v[190:191], v[236:237] op_sel:[1,1] op_sel_hi:[1,0]
	v_pk_fma_f32 v[138:139], v[136:137], v[132:133], 1.0 op_sel_hi:[1,1,0]
	v_pk_fma_f32 v[140:141], v[136:137], v[130:131], 1.0 op_sel_hi:[1,1,0]
	v_pk_fma_f32 v[150:151], v[148:149], v[144:145], 1.0 op_sel_hi:[1,1,0]
	v_pk_fma_f32 v[152:153], v[148:149], v[142:143], 1.0 op_sel_hi:[1,1,0]
	v_pk_fma_f32 v[184:185], v[182:183], v[178:179], 1.0 op_sel_hi:[1,1,0]
	v_pk_fma_f32 v[186:187], v[182:183], v[176:177], 1.0 op_sel_hi:[1,1,0]
	v_pk_fma_f32 v[240:241], v[238:239], v[234:235], 1.0 op_sel_hi:[1,1,0]
	v_pk_fma_f32 v[242:243], v[238:239], v[232:233], 1.0 op_sel_hi:[1,1,0]
	v_cvt_pk_bf16_f32 v154, v138, v139
	v_cvt_pk_bf16_f32 v155, v140, v141
	v_cvt_pk_bf16_f32 v156, v150, v151
	v_cvt_pk_bf16_f32 v157, v152, v153
	v_cvt_pk_bf16_f32 v158, v184, v185
	v_cvt_pk_bf16_f32 v159, v186, v187
	v_cvt_pk_bf16_f32 v160, v240, v241
	v_cvt_pk_bf16_f32 v161, v242, v243
	ds_read_b128 v[22:25], v172 offset:512
	ds_read_b128 v[6:9], v172 offset:576
	ds_read_b128 v[30:33], v172 offset:640
	ds_read_b128 v[14:17], v172 offset:704
	v_permlane16_swap_b32_e32 v154, v156
	v_permlane16_swap_b32_e32 v155, v157
	s_cmp_gt_u32 s40, 7
	s_cbranch_scc1 .Lg1_pl15
	global_store_dwordx4 v228, v[154:157], s[64:65] offset:2048 nt
	s_branch .Lg1_dn15
.Lg1_pl15:
	global_store_dwordx4 v228, v[154:157], s[64:65] offset:2048 sc0 sc1 nt
.Lg1_dn15:
	v_permlane16_swap_b32_e32 v158, v160
	v_permlane16_swap_b32_e32 v159, v161
	s_cmp_gt_u32 s40, 7
	s_cbranch_scc1 .Lg1_pl16
	global_store_dwordx4 v228, v[158:161], s[64:65] offset:2176 nt
	s_branch .Lg1_dn16
.Lg1_pl16:
	global_store_dwordx4 v228, v[158:161], s[64:65] offset:2176 sc0 sc1 nt
.Lg1_dn16:
	v_log_f32_e32 v166, v162
	v_log_f32_e32 v170, v174
	v_add_f32_e32 v168, v164, v165
	v_mul_f32_e32 v168, 0xbeb17218, v168
	v_add_f32_e32 v166, v166, v170
	v_fmac_f32_e32 v168, 0x3f317218, v166
	v_mov_b32_e32 v169, v168
	s_nop 1
	v_permlane16_swap_b32_e32 v168, v169
	v_add_f32_e32 v168, v168, v169
	v_mov_b32_e32 v169, v168
	s_nop 1
	v_permlane32_swap_b32_e32 v168, v169
	v_add_f32_e32 v168, v168, v169
	s_mov_b64 exec, s[0:1]
	global_store_dword v229, v168, s[66:67] offset:576
	s_mov_b64 exec, -1
	s_bitcmp1_b32 s20, 12
	s_cbranch_scc0 .Lg1_noY
	s_barrier
